# HGRN chunk loops: per-step operand loads via saddr + constant 32-bit lane offsets (no per-step 64-bit VALU address math), on top of attention filler address strength reduction + P11 rewrite
# speedup vs baseline: 1.0153x; 1.0069x over previous
; DEV int ltid() { int t = threadIdx.x; asm volatile("" : "+v"(t)); return t; }
; DEV void hgrn_unit(CParams& p, int u, int wg, bool fill) {
;     ...
;   const int sl = u & 3, dir = (u >> 2) & 1, h = (u >> 3) & 7, b = u >> 6;
;   const int tid = ltid(), wid = tid >> 6, lane = tid & 63, fr = lane & 15, fq = lane >> 4;
;   const int dp = lane & 7, seg = lane >> 3, d0 = 16 * wid + 2 * dp;
;   const float* G = dir ? p.gb : p.gf;
;   bf16_t* O = dir ? p.ob : p.of;
;   const int sgn = dir ? -1 : 1;
;     ...
;   f32x4 S[2] = {{0.f, 0.f, 0.f, 0.f}, {0.f, 0.f, 0.f, 0.f}};
;   float dec = 0.f;
;   f32x2 g[8]; unsigned q[8]; u32x2 v;
;   f32x2 gN[8]; unsigned qN[8]; u32x2 vN;
.LBB0_766:
	v_or_b32_e32 v18, v108, v109
	v_mov_b32_e32 v22, v0
	v_add_u32_e32 v194, v18, v116
	v_add_u32_e32 v195, v18, v110
	s_lshl_b32 s21, s24, s21
	s_lshl_b32 s22, s24, 7
	v_ashrrev_i32_e32 v18, 2, v22
	s_and_b32 s21, s21, 0x780
	v_and_b32_e32 v18, -4, v18
	s_and_b32 s22, s22, 0x780
	v_add_u32_e32 v18, s21, v18
	s_or_b32 s25, s22, s3
	v_mad_i64_i32 v[18:19], s[22:23], s20, v18, 0
	v_lshl_add_u64 v[18:19], v[18:19], 2, s[18:19]
	s_lshl_b32 s62, s25, 2
	s_mov_b32 s63, 0
	v_lshl_add_u64 v[20:21], v[18:19], 0, s[62:63]
	v_lshlrev_b32_e32 v18, 4, v22
	v_and_b32_e32 v18, 0xf0, v18
	v_mov_b32_e32 v19, 0
	v_lshl_add_u64 v[20:21], v[20:21], 0, v[18:19]
	s_lshl_b32 s62, s20, 2
	v_lshl_add_u64 v[30:31], v[20:21], 0, s[62:63]
	global_load_dwordx4 v[22:25], v[20:21], off
	global_load_dwordx4 v[26:29], v[30:31], off
	v_lshl_add_u64 v[20:21], v[30:31], 0, s[62:63]
	s_waitcnt lgkmcnt(12)
	v_cndmask_b32_e64 v130, v36, v35, s[12:13]
	v_lshl_add_u64 v[48:49], v[20:21], 0, s[62:63]
	global_load_dwordx4 v[30:33], v[20:21], off
	global_load_dwordx4 v[34:37], v[48:49], off
	s_add_u32 s16, s16, s56
	s_addc_u32 s17, s17, 0
	s_add_u32 s16, s16, s60
	s_addc_u32 s17, s17, 0
	v_mov_b32_e32 v59, v19
	v_lshl_add_u64 v[108:109], s[16:17], 0, v[58:59]
	s_add_u32 s16, s58, s56
	s_addc_u32 s17, s59, 0
	v_ashrrev_i32_e32 v48, 7, v112
	s_add_u32 s16, s16, s60
	v_lshl_or_b32 v18, v48, 4, v113
	s_movk_i32 s62, 0x110
	v_and_b32_e32 v106, 16, v106
	s_addc_u32 s17, s17, 0
	v_mul_lo_u32 v49, v18, s62
	v_lshlrev_b32_e32 v52, 1, v18
	v_mul_lo_u32 v103, v18, s36
	v_lshlrev_b32_e32 v18, 1, v106
	v_or_b32_e32 v47, 3, v102
	v_lshl_add_u64 v[20:21], s[16:17], 0, v[18:19]
	v_lshlrev_b32_e32 v18, 1, v102
	s_add_i32 s16, 0, 0x1e600
	s_add_i32 s61, 0, 0x10400
	s_waitcnt lgkmcnt(0)
	s_barrier
	s_load_dwordx4 s[44:47], s[14:15], 0xe8
	v_add_u32_e32 v202, 0, v49
	v_lshl_add_u64 v[110:111], v[20:21], 0, v[18:19]
	v_add3_u32 v204, s16, v51, v46
	s_load_dwordx2 s[64:65], s[14:15], 0xa0
	s_load_dwordx2 s[66:67], s[14:15], 0xb0
	v_add_u32_e32 v205, s61, v49
	v_or_b32_e32 v21, 64, v114
	v_or_b32_e32 v49, 0x80, v114
	v_or_b32_e32 v51, 0xc0, v114
	v_cmp_gt_u32_e64 s[24:25], v47, v113
	v_or_b32_e32 v47, 32, v46
	s_movk_i32 s26, 0x70
	v_bitop3_b32 v183, v46, v114, 16 bitop3:0x6c
	v_bitop3_b32 v182, v46, v21, 16 bitop3:0x6c
	v_bitop3_b32 v181, v46, v49, 16 bitop3:0x6c
	v_bitop3_b32 v180, v46, v51, 16 bitop3:0x6c
	v_bitop3_b32 v178, v47, v114, 48 bitop3:0x6c
	v_bitop3_b32 v177, v47, v21, 48 bitop3:0x6c
	v_bitop3_b32 v176, v47, v49, 48 bitop3:0x6c
	v_bitop3_b32 v175, v47, v51, 48 bitop3:0x6c
	v_or_b32_e32 v47, 64, v46
	s_movk_i32 s27, 0x50
	v_or_b32_e32 v46, 0x60, v46
	v_or_b32_e32 v53, v106, v113
	v_bitop3_b32 v207, v52, v21, s26 bitop3:0x6c
	v_bitop3_b32 v172, v47, v21, s27 bitop3:0x6c
	v_bitop3_b32 v165, v46, v21, s26 bitop3:0x6c
	v_mov_b32_e32 v21, s80
	v_mul_u32_u24_e32 v203, 0x110, v53
	v_mul_u32_u24_e32 v18, 0x48, v53
	v_add_u32_e32 v20, s16, v114
	s_movk_i32 s14, 0x80
	v_mad_u32_u24 v191, v113, s62, 0
	v_mad_u32_u24 v184, v113, s62, v21
	v_mul_u32_u24_e32 v192, 0x440, v70
	v_mul_u32_u24_e32 v193, 0x110, v50
	v_add_u32_e32 v196, 0x220, v194
	v_add_u32_e32 v197, 0x330, v194
	v_add_u32_e32 v198, 0x440, v194
	v_add_u32_e32 v199, 0x550, v194
	v_add_u32_e32 v200, 0x660, v194
	v_add_u32_e32 v201, 0x770, v194
	s_mov_b32 s57, 4
	v_mul_u32_u24_e32 v187, 0x90, v53
	v_lshl_add_u32 v188, v70, 3, 0
	v_add_u32_e32 v186, 0xfffffc00, v103
	v_bitop3_b32 v206, v52, v114, s26 bitop3:0x6c
	v_bitop3_b32 v208, v52, v49, s26 bitop3:0x6c
	v_bitop3_b32 v209, v52, v51, s26 bitop3:0x6c
	v_cmp_lt_i32_e64 s[16:17], -1, v48
	v_cmp_gt_u32_e64 s[38:39], s14, v112
	v_cmp_gt_u32_e64 s[18:19], v102, v113
	v_cmp_lt_u32_e64 s[20:21], v102, v113
	v_cmp_gt_u32_e64 s[22:23], v50, v113
	v_cmp_lt_i32_e64 s[36:37], 0, v48
	v_add_u32_e32 v190, 0x1100, v191
	v_cmp_eq_u32_e64 s[34:35], 1, v48
	v_cmp_lt_i32_e64 s[14:15], 1, v48
	v_add_u32_e32 v189, 0x2200, v191
	v_bitop3_b32 v173, v47, v114, s27 bitop3:0x6c
	v_bitop3_b32 v171, v47, v49, s27 bitop3:0x6c
	v_bitop3_b32 v170, v47, v51, s27 bitop3:0x6c
	v_cmp_eq_u32_e64 s[30:31], 2, v48
	v_cmp_lt_i32_e64 s[28:29], 2, v48
	v_bitop3_b32 v167, v46, v114, s26 bitop3:0x6c
	v_bitop3_b32 v164, v46, v49, s26 bitop3:0x6c
	v_bitop3_b32 v163, v46, v51, s26 bitop3:0x6c
	v_cmp_eq_u32_e64 s[26:27], 3, v48
	v_add_u32_e32 v179, 0x1100, v184
	v_add_u32_e32 v174, 0x2200, v184
	v_add_u32_e32 v166, 0x3300, v184
	v_add_lshl_u32 v210, v18, v102, 1
	s_add_i32 s82, s2, 0x700
	s_movk_i32 s83, 0x84
	s_movk_i32 s84, 0x7ff
	s_mov_b32 s85, 0xda24260
	v_mov_b32_e32 v211, 0xfffff800
	v_mov_b32_e32 v212, 0x80
	v_mov_b32_e32 v213, 0x7149f2ca
	v_add_u32_e32 v160, v20, v203
	s_mov_b32 s86, 0
	s_mov_b32 s87, 0
	v_readfirstlane_b32 s32, v82
	v_readfirstlane_b32 s92, v83
	v_readfirstlane_b32 s93, v84
	v_readfirstlane_b32 s94, v85
	v_readfirstlane_b32 s95, v108
	v_readfirstlane_b32 s96, v109
	s_nop 1
	v_subrev_u32_e32 v82, s32, v82
	v_add_u32_e32 v82, 0x40000, v82
	v_subrev_u32_e32 v108, s95, v108
	v_add_u32_e32 v108, 0x20000, v108
	v_lshl_add_u32 v151, v151, 12, v82
	v_lshl_add_u32 v135, v135, 12, v82
	v_lshl_add_u32 v136, v136, 12, v82
	v_lshl_add_u32 v137, v137, 12, v82
	v_lshl_add_u32 v138, v138, 12, v82
	v_lshl_add_u32 v139, v139, 12, v82
	v_lshl_add_u32 v141, v141, 12, v82
	v_lshl_add_u32 v143, v143, 12, v82
	v_lshl_add_u32 v144, v144, 11, v108
	s_branch .LBB0_770

.LBB0_770:
	s_add_i32 s88, s77, s87
	s_add_i32 s89, s77, s86
	s_add_i32 s62, s88, 0x137f
	s_add_i32 s70, s89, 0x480
	s_and_b64 s[68:69], s[52:53], exec
	s_cselect_b32 s62, s70, s62
	s_sub_u32 s70, s62, 64
	s_lshl_b32 s72, s70, 11
	s_lshl_b32 s70, s70, 12
	s_add_u32 s70, s32, s70
	s_addc_u32 s71, s92, 0
	s_add_u32 s72, s93, s72
	s_addc_u32 s73, s94, 0
	v_lshrrev_b32_e32 v20, 1, v151
	global_load_dword v250, v20, s[72:73]
	global_load_dwordx2 v[126:127], v151, s[70:71]
	v_lshrrev_b32_e32 v21, 1, v135
	global_load_dword v249, v21, s[72:73]
	global_load_dwordx2 v[124:125], v135, s[70:71]
	v_lshrrev_b32_e32 v20, 1, v136
	global_load_dword v248, v20, s[72:73]
	global_load_dwordx2 v[122:123], v136, s[70:71]
	v_lshrrev_b32_e32 v21, 1, v137
	global_load_dword v247, v21, s[72:73]
	global_load_dwordx2 v[120:121], v137, s[70:71]
	v_lshrrev_b32_e32 v20, 1, v138
	global_load_dword v242, v20, s[72:73]
	global_load_dwordx2 v[118:119], v138, s[70:71]
	v_lshrrev_b32_e32 v21, 1, v139
	global_load_dword v240, v21, s[72:73]
	global_load_dwordx2 v[116:117], v139, s[70:71]
	v_lshrrev_b32_e32 v20, 1, v141
	global_load_dword v239, v20, s[72:73]
	global_load_dwordx2 v[114:115], v141, s[70:71]
	v_lshrrev_b32_e32 v21, 1, v143
	global_load_dword v238, v21, s[72:73]
	global_load_dwordx2 v[112:113], v143, s[70:71]
	s_sub_u32 s70, s62, 64
	s_lshl_b32 s70, s70, 11
	s_add_u32 s70, s95, s70
	s_addc_u32 s71, s96, 0
	global_load_dwordx2 v[128:129], v144, s[70:71]
	s_add_i32 s91, s82, 0xfffffc00
	s_ashr_i32 s90, s91, 1
	s_cmpk_lt_i32 s90, 0x4000
	v_mov_b32_e32 v18, v0
	s_cselect_b64 s[70:71], -1, 0
	s_cmpk_gt_i32 s90, 0x3fff
	s_mov_b64 s[72:73], -1
	s_cbranch_scc0 .LBB0_772
	s_add_i32 s62, s90, 0xffffc000
	s_lshr_b32 s62, s62, 8
	s_lshl_b64 s[68:69], s[62:63], 22
	s_waitcnt lgkmcnt(0)
	s_add_u32 s68, s46, s68
	s_addc_u32 s69, s47, s69
	s_mov_b64 s[72:73], 0

; DEV int ltid() { int t = threadIdx.x; asm volatile("" : "+v"(t)); return t; }
; DEV void fill_load(CParams& p, int wg, int slot, f32x4 (&ld)[4]) {
;   const FillDesc d = fill_decode(p, wg, slot); const int tid = ltid(), tx = tid & 15, ty = tid >> 4;
;   const float* sp = d.src + (long)(d.kh + 4 * ty) * d.ldsrc + d.n0 + 4 * tx;
; #pragma unroll
;   for (int r = 0; r < 4; ++r) ld[r] = *(const f32x4*)(sp + (long)r * d.ldsrc);
; }
.LBB0_801:
	v_mov_b32_e32 v4, v0
	s_lshl_b32 s62, s72, s62
	s_lshl_b32 s71, s72, 7
	v_ashrrev_i32_e32 v2, 2, v4
	s_and_b32 s62, s62, 0x780
	v_and_b32_e32 v2, -4, v2
	s_and_b32 s71, s71, 0x780
	v_add_u32_e32 v2, s62, v2
	s_or_b32 s71, s71, s3
	v_mad_i64_i32 v[2:3], s[72:73], s70, v2, 0
	v_lshl_add_u64 v[2:3], v[2:3], 2, s[68:69]
	s_lshl_b32 s62, s71, 2
	v_lshlrev_b32_e32 v4, 4, v4
	v_lshl_add_u64 v[2:3], v[2:3], 0, s[62:63]
	v_and_b32_e32 v18, 0xf0, v4
	v_lshl_add_u64 v[2:3], v[2:3], 0, v[18:19]
	s_lshl_b32 s62, s70, 2
	v_lshl_add_u64 v[4:5], v[2:3], 0, s[62:63]
	global_load_dwordx4 v[10:13], v[2:3], off
	global_load_dwordx4 v[14:17], v[4:5], off
	v_lshl_add_u64 v[2:3], v[4:5], 0, s[62:63]
	v_lshl_add_u64 v[6:7], v[2:3], 0, s[62:63]
	s_add_i32 s62, s88, 0x133f
	s_add_i32 s70, s89, 0x4c0
	s_and_b64 s[68:69], s[52:53], exec
	s_cselect_b32 s62, s70, s62
	s_sub_u32 s70, s62, 64
	s_lshl_b32 s72, s70, 11
	s_lshl_b32 s70, s70, 12
	s_add_u32 s70, s32, s70
	s_addc_u32 s71, s92, 0
	s_add_u32 s72, s93, s72
	s_addc_u32 s73, s94, 0
	global_load_dwordx4 v[2:5], v[2:3], off
	s_nop 0
	global_load_dwordx4 v[6:9], v[6:7], off
	s_waitcnt lgkmcnt(0)
	s_barrier
	v_lshrrev_b32_e32 v20, 1, v151
	global_load_dword v169, v20, s[72:73]
	global_load_dwordx2 v[100:101], v151, s[70:71]
	v_lshrrev_b32_e32 v21, 1, v135
	global_load_dword v168, v21, s[72:73]
	global_load_dwordx2 v[98:99], v135, s[70:71]
	v_lshrrev_b32_e32 v20, 1, v136
	global_load_dword v162, v20, s[72:73]
	global_load_dwordx2 v[96:97], v136, s[70:71]
	v_lshrrev_b32_e32 v21, 1, v137
	global_load_dword v161, v21, s[72:73]
	global_load_dwordx2 v[94:95], v137, s[70:71]
	v_lshrrev_b32_e32 v20, 1, v138
	global_load_dword v159, v20, s[72:73]
	global_load_dwordx2 v[92:93], v138, s[70:71]
	v_lshrrev_b32_e32 v21, 1, v139
	global_load_dword v158, v21, s[72:73]
	global_load_dwordx2 v[90:91], v139, s[70:71]
	v_lshrrev_b32_e32 v20, 1, v141
	global_load_dword v157, v20, s[72:73]
	global_load_dwordx2 v[88:89], v141, s[70:71]
	v_lshrrev_b32_e32 v21, 1, v143
	global_load_dword v156, v21, s[72:73]
	global_load_dwordx2 v[86:87], v143, s[70:71]
	s_sub_u32 s70, s62, 64
	s_lshl_b32 s70, s70, 11
	s_add_u32 s70, s95, s70
	s_addc_u32 s71, s96, 0
	global_load_dwordx2 v[104:105], v144, s[70:71]
	s_add_i32 s91, s82, 0xfffffd00
	s_ashr_i32 s90, s91, 1
	s_cmpk_lt_i32 s90, 0x4000
	v_mov_b32_e32 v18, v0
	s_cselect_b64 s[70:71], -1, 0
	s_cmpk_gt_i32 s90, 0x3fff
	s_mov_b64 s[72:73], -1
	s_cbranch_scc0 .LBB0_803
	s_add_i32 s62, s90, 0xffffc000
	s_lshr_b32 s62, s62, 8
	s_lshl_b64 s[68:69], s[62:63], 22
	s_add_u32 s68, s46, s68
	s_addc_u32 s69, s47, s69
	s_mov_b64 s[72:73], 0

; DEV int ltid() { int t = threadIdx.x; asm volatile("" : "+v"(t)); return t; }
; DEV void hgrn_unit(CParams& p, int u, int wg, bool fill) {
;     ...
;   const int sl = u & 3, dir = (u >> 2) & 1, h = (u >> 3) & 7, b = u >> 6;
;   const int tid = ltid(), wid = tid >> 6, lane = tid & 63, fr = lane & 15, fq = lane >> 4;
;   const int dp = lane & 7, seg = lane >> 3, d0 = 16 * wid + 2 * dp;
;   const float* G = dir ? p.gb : p.gf;
;   bf16_t* O = dir ? p.ob : p.of;
;   const int sgn = dir ? -1 : 1;
;     ...
;   f32x4 S[2] = {{0.f, 0.f, 0.f, 0.f}, {0.f, 0.f, 0.f, 0.f}};
;   float dec = 0.f;
;   f32x2 g[8]; unsigned q[8]; u32x2 v;
;   f32x2 gN[8]; unsigned qN[8]; u32x2 vN;
.LBB0_971:
	v_or_b32_e32 v18, v108, v109
	v_mov_b32_e32 v22, v0
	v_add_u32_e32 v195, v18, v116
	v_add_u32_e32 v196, v18, v111
	s_lshl_b32 s21, s25, s21
	s_lshl_b32 s22, s25, 7
	v_ashrrev_i32_e32 v18, 2, v22
	s_and_b32 s21, s21, 0x780
	v_and_b32_e32 v18, -4, v18
	s_and_b32 s22, s24, s22
	v_add_u32_e32 v18, s21, v18
	s_or_b32 s24, s22, s53
	v_mad_i64_i32 v[18:19], s[22:23], s20, v18, 0
	v_lshl_add_u64 v[18:19], v[18:19], 2, s[18:19]
	s_lshl_b32 s62, s24, 2
	s_mov_b32 s63, 0
	v_lshl_add_u64 v[20:21], v[18:19], 0, s[62:63]
	v_lshlrev_b32_e32 v18, 4, v22
	v_and_b32_e32 v18, 0xf0, v18
	v_mov_b32_e32 v19, 0
	v_lshl_add_u64 v[20:21], v[20:21], 0, v[18:19]
	s_lshl_b32 s62, s20, 2
	v_lshl_add_u64 v[30:31], v[20:21], 0, s[62:63]
	global_load_dwordx4 v[22:25], v[20:21], off
	global_load_dwordx4 v[26:29], v[30:31], off
	v_lshl_add_u64 v[20:21], v[30:31], 0, s[62:63]
	s_waitcnt lgkmcnt(12)
	v_cndmask_b32_e64 v130, v36, v35, s[12:13]
	v_lshl_add_u64 v[48:49], v[20:21], 0, s[62:63]
	global_load_dwordx4 v[30:33], v[20:21], off
	global_load_dwordx4 v[34:37], v[48:49], off
	s_add_u32 s16, s16, s56
	s_addc_u32 s17, s17, 0
	s_add_u32 s16, s16, s60
	s_addc_u32 s17, s17, 0
	v_mov_b32_e32 v59, v19
	v_lshl_add_u64 v[108:109], s[16:17], 0, v[58:59]
	s_add_u32 s16, s58, s56
	s_addc_u32 s17, s59, 0
	v_ashrrev_i32_e32 v48, 7, v112
	s_add_u32 s16, s16, s60
	v_lshl_or_b32 v18, v48, 4, v113
	s_movk_i32 s62, 0x110
	v_and_b32_e32 v106, 16, v110
	s_addc_u32 s17, s17, 0
	v_mul_lo_u32 v49, v18, s62
	v_lshlrev_b32_e32 v52, 1, v18
	v_mul_lo_u32 v107, v18, s36
	v_lshlrev_b32_e32 v18, 1, v106
	v_or_b32_e32 v47, 3, v254
	v_lshl_add_u64 v[20:21], s[16:17], 0, v[18:19]
	v_lshlrev_b32_e32 v18, 1, v254
	s_add_i32 s16, 0, 0x1e600
	s_add_i32 s61, 0, 0x10400
	s_waitcnt lgkmcnt(0)
	s_barrier
	s_load_dwordx4 s[44:47], s[14:15], 0xe8
	v_add_u32_e32 v203, 0, v49
	v_lshl_add_u64 v[110:111], v[20:21], 0, v[18:19]
	v_add3_u32 v205, s16, v51, v46
	s_load_dwordx2 s[64:65], s[14:15], 0xa0
	s_load_dwordx2 s[66:67], s[14:15], 0xb0
	v_add_u32_e32 v206, s61, v49
	v_or_b32_e32 v21, 64, v115
	v_or_b32_e32 v49, 0x80, v115
	v_or_b32_e32 v51, 0xc0, v115
	v_cmp_gt_u32_e64 s[24:25], v47, v113
	v_or_b32_e32 v47, 32, v46
	s_movk_i32 s26, 0x70
	v_bitop3_b32 v184, v46, v115, 16 bitop3:0x6c
	v_bitop3_b32 v183, v46, v21, 16 bitop3:0x6c
	v_bitop3_b32 v182, v46, v49, 16 bitop3:0x6c
	v_bitop3_b32 v181, v46, v51, 16 bitop3:0x6c
	v_bitop3_b32 v179, v47, v115, 48 bitop3:0x6c
	v_bitop3_b32 v178, v47, v21, 48 bitop3:0x6c
	v_bitop3_b32 v177, v47, v49, 48 bitop3:0x6c
	v_bitop3_b32 v176, v47, v51, 48 bitop3:0x6c
	v_or_b32_e32 v47, 64, v46
	s_movk_i32 s27, 0x50
	v_or_b32_e32 v46, 0x60, v46
	v_or_b32_e32 v53, v106, v113
	v_bitop3_b32 v208, v52, v21, s26 bitop3:0x6c
	v_bitop3_b32 v173, v47, v21, s27 bitop3:0x6c
	v_bitop3_b32 v166, v46, v21, s26 bitop3:0x6c
	v_mov_b32_e32 v21, s81
	v_mul_u32_u24_e32 v204, 0x110, v53
	v_mul_u32_u24_e32 v18, 0x48, v53
	v_add_u32_e32 v20, s16, v115
	s_movk_i32 s14, 0x80
	v_mad_u32_u24 v192, v113, s62, 0
	v_mad_u32_u24 v185, v113, s62, v21
	v_mul_u32_u24_e32 v193, 0x440, v70
	v_mul_u32_u24_e32 v194, 0x110, v50
	v_add_u32_e32 v197, 0x220, v195
	v_add_u32_e32 v198, 0x330, v195
	v_add_u32_e32 v199, 0x440, v195
	v_add_u32_e32 v200, 0x550, v195
	v_add_u32_e32 v201, 0x660, v195
	v_add_u32_e32 v202, 0x770, v195
	s_mov_b32 s57, 4
	v_mul_u32_u24_e32 v188, 0x90, v53
	v_lshl_add_u32 v189, v70, 3, 0
	v_add_u32_e32 v187, 0xfffffc00, v107
	v_bitop3_b32 v207, v52, v115, s26 bitop3:0x6c
	v_bitop3_b32 v209, v52, v49, s26 bitop3:0x6c
	v_bitop3_b32 v210, v52, v51, s26 bitop3:0x6c
	v_cmp_lt_i32_e64 s[16:17], -1, v48
	v_cmp_gt_u32_e64 s[38:39], s14, v112
	v_cmp_gt_u32_e64 s[18:19], v254, v113
	v_cmp_lt_u32_e64 s[20:21], v254, v113
	v_cmp_gt_u32_e64 s[22:23], v50, v113
	v_cmp_lt_i32_e64 s[36:37], 0, v48
	v_add_u32_e32 v191, 0x1100, v192
	v_cmp_eq_u32_e64 s[34:35], 1, v48
	v_cmp_lt_i32_e64 s[14:15], 1, v48
	v_add_u32_e32 v190, 0x2200, v192
	v_bitop3_b32 v174, v47, v115, s27 bitop3:0x6c
	v_bitop3_b32 v172, v47, v49, s27 bitop3:0x6c
	v_bitop3_b32 v171, v47, v51, s27 bitop3:0x6c
	v_cmp_eq_u32_e64 s[30:31], 2, v48
	v_cmp_lt_i32_e64 s[28:29], 2, v48
	v_bitop3_b32 v169, v46, v115, s26 bitop3:0x6c
	v_bitop3_b32 v165, v46, v49, s26 bitop3:0x6c
	v_bitop3_b32 v164, v46, v51, s26 bitop3:0x6c
	v_cmp_eq_u32_e64 s[26:27], 3, v48
	v_add_u32_e32 v180, 0x1100, v185
	v_add_u32_e32 v175, 0x2200, v185
	v_add_u32_e32 v168, 0x3300, v185
	v_add_lshl_u32 v211, v18, v254, 1
	s_add_i32 s83, s2, 0x700
	s_movk_i32 s84, 0x84
	s_movk_i32 s85, 0x7ff
	s_mov_b32 s86, 0xda24260
	v_mov_b32_e32 v212, 0xfffff800
	v_mov_b32_e32 v213, 0x80
	v_mov_b32_e32 v214, 0x7149f2ca
	v_add_u32_e32 v162, v20, v204
	s_mov_b32 s87, 0
	s_mov_b32 s88, 0
	v_readfirstlane_b32 s32, v84
	v_readfirstlane_b32 s93, v85
	v_readfirstlane_b32 s94, v86
	v_readfirstlane_b32 s95, v87
	v_readfirstlane_b32 s96, v108
	v_readfirstlane_b32 s97, v109
	s_nop 1
	v_subrev_u32_e32 v84, s32, v84
	v_add_u32_e32 v84, 0x40000, v84
	v_subrev_u32_e32 v108, s96, v108
	v_add_u32_e32 v108, 0x20000, v108
	v_lshl_add_u32 v152, v152, 12, v84
	v_lshl_add_u32 v136, v136, 12, v84
	v_lshl_add_u32 v137, v137, 12, v84
	v_lshl_add_u32 v138, v138, 12, v84
	v_lshl_add_u32 v139, v139, 12, v84
	v_lshl_add_u32 v140, v140, 12, v84
	v_lshl_add_u32 v142, v142, 12, v84
	v_lshl_add_u32 v144, v144, 12, v84
	v_lshl_add_u32 v145, v145, 11, v108
	s_branch .LBB0_975

.LBB0_975:
	s_add_i32 s89, s79, s88
	s_add_i32 s90, s79, s87
	s_add_i32 s62, s89, 0x137f
	s_add_i32 s70, s90, 0x480
	s_and_b64 s[68:69], s[54:55], exec
	s_cselect_b32 s62, s70, s62
	s_sub_u32 s70, s62, 64
	s_lshl_b32 s72, s70, 11
	s_lshl_b32 s70, s70, 12
	s_add_u32 s70, s32, s70
	s_addc_u32 s71, s93, 0
	s_add_u32 s72, s94, s72
	s_addc_u32 s73, s95, 0
	v_lshrrev_b32_e32 v20, 1, v152
	global_load_dword v251, v20, s[72:73] offset:1024
	global_load_dwordx2 v[126:127], v152, s[70:71] offset:2048
	v_lshrrev_b32_e32 v21, 1, v136
	global_load_dword v250, v21, s[72:73] offset:1024
	global_load_dwordx2 v[124:125], v136, s[70:71] offset:2048
	v_lshrrev_b32_e32 v20, 1, v137
	global_load_dword v249, v20, s[72:73] offset:1024
	global_load_dwordx2 v[122:123], v137, s[70:71] offset:2048
	v_lshrrev_b32_e32 v21, 1, v138
	global_load_dword v248, v21, s[72:73] offset:1024
	global_load_dwordx2 v[120:121], v138, s[70:71] offset:2048
	v_lshrrev_b32_e32 v20, 1, v139
	global_load_dword v247, v20, s[72:73] offset:1024
	global_load_dwordx2 v[118:119], v139, s[70:71] offset:2048
	v_lshrrev_b32_e32 v21, 1, v140
	global_load_dword v246, v21, s[72:73] offset:1024
	global_load_dwordx2 v[116:117], v140, s[70:71] offset:2048
	v_lshrrev_b32_e32 v20, 1, v142
	global_load_dword v241, v20, s[72:73] offset:1024
	global_load_dwordx2 v[114:115], v142, s[70:71] offset:2048
	v_lshrrev_b32_e32 v21, 1, v144
	global_load_dword v239, v21, s[72:73] offset:1024
	global_load_dwordx2 v[112:113], v144, s[70:71] offset:2048
	s_sub_u32 s70, s62, 64
	s_lshl_b32 s70, s70, 11
	s_add_u32 s70, s96, s70
	s_addc_u32 s71, s97, 0
	global_load_dwordx2 v[128:129], v145, s[70:71] offset:1024
	s_add_i32 s92, s83, 0xfffffc00
	s_ashr_i32 s91, s92, 1
	s_cmpk_lt_i32 s91, 0x4000
	v_mov_b32_e32 v18, v0
	s_cselect_b64 s[70:71], -1, 0
	s_cmpk_gt_i32 s91, 0x3fff
	s_mov_b64 s[72:73], -1
	s_cbranch_scc0 .LBB0_977
	s_add_i32 s62, s91, 0xffffc000
	s_lshr_b32 s62, s62, 8
	s_lshl_b64 s[68:69], s[62:63], 22
	s_waitcnt lgkmcnt(0)
	s_add_u32 s68, s46, s68
	s_addc_u32 s69, s47, s69
	s_mov_b64 s[72:73], 0

; DEV int ltid() { int t = threadIdx.x; asm volatile("" : "+v"(t)); return t; }
; DEV void fill_load(CParams& p, int wg, int slot, f32x4 (&ld)[4]) {
;   const FillDesc d = fill_decode(p, wg, slot); const int tid = ltid(), tx = tid & 15, ty = tid >> 4;
;   const float* sp = d.src + (long)(d.kh + 4 * ty) * d.ldsrc + d.n0 + 4 * tx;
; #pragma unroll
;   for (int r = 0; r < 4; ++r) ld[r] = *(const f32x4*)(sp + (long)r * d.ldsrc);
; }
.LBB0_1007:
	v_mov_b32_e32 v4, v0
	s_lshl_b32 s62, s72, s62
	s_lshl_b32 s73, s72, 7
	v_ashrrev_i32_e32 v2, 2, v4
	s_and_b32 s62, s62, 0x780
	v_and_b32_e32 v2, -4, v2
	s_and_b32 s71, s71, s73
	v_add_u32_e32 v2, s62, v2
	s_or_b32 s71, s71, s53
	v_mad_i64_i32 v[2:3], s[72:73], s70, v2, 0
	v_lshl_add_u64 v[2:3], v[2:3], 2, s[68:69]
	s_lshl_b32 s62, s71, 2
	v_lshlrev_b32_e32 v4, 4, v4
	v_lshl_add_u64 v[2:3], v[2:3], 0, s[62:63]
	v_and_b32_e32 v18, 0xf0, v4
	v_lshl_add_u64 v[2:3], v[2:3], 0, v[18:19]
	s_lshl_b32 s62, s70, 2
	v_lshl_add_u64 v[4:5], v[2:3], 0, s[62:63]
	global_load_dwordx4 v[10:13], v[2:3], off
	global_load_dwordx4 v[14:17], v[4:5], off
	v_lshl_add_u64 v[2:3], v[4:5], 0, s[62:63]
	v_lshl_add_u64 v[6:7], v[2:3], 0, s[62:63]
	s_add_i32 s62, s89, 0x133f
	s_add_i32 s70, s90, 0x4c0
	s_and_b64 s[68:69], s[54:55], exec
	s_cselect_b32 s62, s70, s62
	s_sub_u32 s70, s62, 64
	s_lshl_b32 s72, s70, 11
	s_lshl_b32 s70, s70, 12
	s_add_u32 s70, s32, s70
	s_addc_u32 s71, s93, 0
	s_add_u32 s72, s94, s72
	s_addc_u32 s73, s95, 0
	global_load_dwordx4 v[2:5], v[2:3], off
	s_nop 0
	global_load_dwordx4 v[6:9], v[6:7], off
	s_waitcnt lgkmcnt(0)
	s_barrier
	v_lshrrev_b32_e32 v20, 1, v152
	global_load_dword v170, v20, s[72:73] offset:1024
	global_load_dwordx2 v[102:103], v152, s[70:71] offset:2048
	v_lshrrev_b32_e32 v21, 1, v136
	global_load_dword v167, v21, s[72:73] offset:1024
	global_load_dwordx2 v[100:101], v136, s[70:71] offset:2048
	v_lshrrev_b32_e32 v20, 1, v137
	global_load_dword v163, v20, s[72:73] offset:1024
	global_load_dwordx2 v[98:99], v137, s[70:71] offset:2048
	v_lshrrev_b32_e32 v21, 1, v138
	global_load_dword v161, v21, s[72:73] offset:1024
	global_load_dwordx2 v[96:97], v138, s[70:71] offset:2048
	v_lshrrev_b32_e32 v20, 1, v139
	global_load_dword v160, v20, s[72:73] offset:1024
	global_load_dwordx2 v[94:95], v139, s[70:71] offset:2048
	v_lshrrev_b32_e32 v21, 1, v140
	global_load_dword v159, v21, s[72:73] offset:1024
	global_load_dwordx2 v[92:93], v140, s[70:71] offset:2048
	v_lshrrev_b32_e32 v20, 1, v142
	global_load_dword v158, v20, s[72:73] offset:1024
	global_load_dwordx2 v[90:91], v142, s[70:71] offset:2048
	v_lshrrev_b32_e32 v21, 1, v144
	global_load_dword v157, v21, s[72:73] offset:1024
	global_load_dwordx2 v[88:89], v144, s[70:71] offset:2048
	s_sub_u32 s70, s62, 64
	s_lshl_b32 s70, s70, 11
	s_add_u32 s70, s96, s70
	s_addc_u32 s71, s97, 0
	global_load_dwordx2 v[104:105], v145, s[70:71] offset:1024
	s_add_i32 s92, s83, 0xfffffd00
	s_ashr_i32 s91, s92, 1
	s_cmpk_lt_i32 s91, 0x4000
	v_mov_b32_e32 v18, v0
	s_cselect_b64 s[70:71], -1, 0
	s_cmpk_gt_i32 s91, 0x3fff
	s_mov_b64 s[72:73], -1
	s_cbranch_scc0 .LBB0_1009
	s_add_i32 s62, s91, 0xffffc000
	s_lshr_b32 s62, s62, 8
	s_lshl_b64 s[68:69], s[62:63], 22
	s_add_u32 s68, s46, s68
	s_addc_u32 s69, s47, s69
	s_mov_b64 s[72:73], 0
